# streaming hint (nt) on the read-once loads of two memory phases: norm2's residual-row loads and the f32 expert weights in the weight conversion; plus previous changes
# speedup vs baseline: 1.0114x; 1.0020x over previous
;     __device__ __forceinline__ float* mods() const { return (float*)(ws + WS_MODS); }
; __device__ __forceinline__ void phase_norm2_route(const Frame& F, const Params& P, int l, int nrows, long long dctx) {
;     ...
;     for (int rowA = r0 + F.wid; rowA < r1; rowA += 16) {
;         const int rowB = rowA + 8; const bool hasB = rowB < r1; const int rowBs = hasB ? rowB : rowA;
;         const float* xa = xrow_ptr(P.out, dctx, rowA); const float* xb = xrow_ptr(P.out, dctx, rowBs);
;         f32x4 va[4], vb[4]; float sa = 0.f, sb = 0.f;
; #pragma unroll
;         for (int j = 0; j < 4; ++j) { va[j] = *(const f32x4*)(xa + F.lane * 4 + 256 * j); vb[j] = *(const f32x4*)(xb + F.lane * 4 + 256 * j); }
; #pragma unroll
;         for (int j = 0; j < 4; ++j) { sa += va[j][0] * va[j][0] + va[j][1] * va[j][1] + va[j][2] * va[j][2] + va[j][3] * va[j][3]; sb += vb[j][0] * vb[j][0] + vb[j][1] * vb[j][1] + vb[j][2] * vb[j][2] + vb[j][3] * vb[j][3]; }
;         sa = wave_sum(sa); sb = wave_sum(sb);
;         const float ra = rsqrtf(sa * (1.f / 1024.f) + EPS), rb = rsqrtf(sb * (1.f / 1024.f) + EPS);
;         const float* mda = F.mods() + (size_t)(l * 9 + (rowA < TL ? (rowA >> 13) : 8)) * 6144;
;         const float* mdb = F.mods() + (size_t)(l * 9 + (rowBs < TL ? (rowBs >> 13) : 8)) * 6144;
; #pragma unroll
;         for (int j = 0; j < 4; ++j) {
;             const int col = F.lane * 4 + 256 * j;
;             const f32x4 gg = *(const f32x4*)(g + col);
;             const f32x4 sha = *(const f32x4*)(mda + 3 * 1024 + col), sca = *(const f32x4*)(mda + 4 * 1024 + col);
;             const f32x4 shb = *(const f32x4*)(mdb + 3 * 1024 + col), scb = *(const f32x4*)(mdb + 4 * 1024 + col);
.LBB0_925:
	s_add_i32 s18, s0, 8
	s_cmp_lt_i32 s18, s85
	s_cselect_b64 s[28:29], -1, 0
	s_and_b64 s[8:9], s[28:29], exec
	s_cselect_b32 s8, s18, s0
	s_cmp_gt_i32 s0, 0xffff
	s_cselect_b32 s22, s60, 0
	s_cselect_b32 s23, s61, 0
	s_ashr_i32 s9, s8, 31
	v_lshl_add_u64 v[2:3], s[22:23], 2, v[34:35]
	s_lshl_b64 s[22:23], s[8:9], 12
	global_load_dwordx4 v[26:29], v[2:3], off nt
	global_load_dwordx4 v[22:25], v[2:3], off offset:1024 nt
	global_load_dwordx4 v[14:17], v[2:3], off offset:2048 nt
	s_nop 0
	global_load_dwordx4 v[2:5], v[2:3], off offset:3072 nt
	s_add_u32 s9, s36, s22
	s_addc_u32 s19, s37, s23
	s_cmp_gt_i32 s8, 0xffff
	s_cselect_b32 s23, s61, 0
	s_cselect_b32 s22, s60, 0
	s_lshl_b64 s[22:23], s[22:23], 2
	s_add_u32 s22, s9, s22
	s_addc_u32 s23, s19, s23
	global_load_dwordx4 v[44:47], v1, s[22:23] nt
	global_load_dwordx4 v[18:21], v1, s[22:23] offset:1024 nt
	global_load_dwordx4 v[10:13], v1, s[22:23] offset:2048 nt
	global_load_dwordx4 v[6:9], v1, s[22:23] offset:3072 nt
	global_load_dwordx4 v[48:51], v[32:33], off
	s_min_i32 s9, s0, 0x10000
	s_ashr_i32 s9, s9, 13
	s_add_i32 s9, s9, s1
	s_mul_hi_i32 s19, s9, 0x6000
	s_mulk_i32 s9, 0x6000
	s_add_u32 s9, s2, s9
	s_addc_u32 s19, s7, s19
	s_min_i32 s8, s8, 0x10000
	s_ashr_i32 s8, s8, 13
	s_add_i32 s8, s8, s1
	s_mul_hi_i32 s22, s8, 0x6000
	s_mulk_i32 s8, 0x6000
	s_add_u32 s8, s2, s8
	s_addc_u32 s22, s7, s22
	s_add_u32 s48, s9, 0x3000
	s_addc_u32 s49, s19, 0
	s_add_u32 s52, s9, 0x4000
	s_addc_u32 s53, s19, 0
	s_add_u32 s50, s8, 0x3000
	global_load_dwordx4 v[52:55], v1, s[48:49]
	global_load_dwordx4 v[56:59], v1, s[52:53]
	s_addc_u32 s51, s22, 0
	s_add_u32 s54, s8, 0x4000
	s_addc_u32 s55, s22, 0
	global_load_dwordx4 v[60:63], v1, s[50:51]
	global_load_dwordx4 v[64:67], v1, s[54:55]
	s_mov_b32 s8, 0x3a800000
	s_cmp_ge_i32 s18, s85
	global_load_dwordx4 v[68:71], v[32:33], off offset:1024
	global_load_dwordx4 v[72:75], v38, s[48:49]
	global_load_dwordx4 v[76:79], v38, s[52:53]
	global_load_dwordx4 v[80:83], v38, s[50:51]
	global_load_dwordx4 v[84:87], v38, s[54:55]
	global_load_dwordx4 v[88:91], v[32:33], off offset:2048
	global_load_dwordx4 v[92:95], v39, s[48:49]
	global_load_dwordx4 v[96:99], v39, s[52:53]
	global_load_dwordx4 v[100:103], v39, s[50:51]
	global_load_dwordx4 v[104:107], v39, s[54:55]
	global_load_dwordx4 v[108:111], v[32:33], off offset:3072
	global_load_dwordx4 v[112:115], v40, s[52:53]
	global_load_dwordx4 v[116:119], v40, s[54:55]
	global_load_dwordx4 v[120:123], v40, s[48:49]
	global_load_dwordx4 v[124:127], v40, s[50:51]
	s_waitcnt vmcnt(15)
; __device__ __forceinline__ unsigned cvt_pk_bf16(float lo, float hi) { unsigned r; asm volatile("v_cvt_pk_bf16_f32 %0, %1, %2" : "=v"(r) : "v"(lo), "v"(hi)); return r; }
; __device__ __forceinline__ float bf_lo(unsigned w) { return __uint_as_float(w << 16); }
; __device__ __forceinline__ float bf_hi(unsigned w) { return __uint_as_float(w & 0xffff0000u); }
; __device__ __forceinline__ void phase_norm2_route(const Frame& F, const Params& P, int l, int nrows, long long dctx) {
;     ...
; #pragma unroll
;         for (int j = 0; j < 4; ++j) { sa += va[j][0] * va[j][0] + va[j][1] * va[j][1] + va[j][2] * va[j][2] + va[j][3] * va[j][3]; sb += vb[j][0] * vb[j][0] + vb[j][1] * vb[j][1] + vb[j][2] * vb[j][2] + vb[j][3] * vb[j][3]; }
;         sa = wave_sum(sa); sb = wave_sum(sb);
;         const float ra = rsqrtf(sa * (1.f / 1024.f) + EPS), rb = rsqrtf(sb * (1.f / 1024.f) + EPS);
;         const float* mda = F.mods() + (size_t)(l * 9 + (rowA < TL ? (rowA >> 13) : 8)) * 6144;
;         const float* mdb = F.mods() + (size_t)(l * 9 + (rowBs < TL ? (rowBs >> 13) : 8)) * 6144;
; #pragma unroll
;         for (int j = 0; j < 4; ++j) {
;             const int col = F.lane * 4 + 256 * j;
;             const f32x4 gg = *(const f32x4*)(g + col);
;             const f32x4 sha = *(const f32x4*)(mda + 3 * 1024 + col), sca = *(const f32x4*)(mda + 4 * 1024 + col);
;             const f32x4 shb = *(const f32x4*)(mdb + 3 * 1024 + col), scb = *(const f32x4*)(mdb + 4 * 1024 + col);
;             float oa[4], ob[4];
; #pragma unroll
;             for (int i = 0; i < 4; ++i) { oa[i] = va[j][i] * ra * gg[i] * (1.f + sca[i]) + sha[i]; ob[i] = vb[j][i] * rb * gg[i] * (1.f + scb[i]) + shb[i]; }
;             u32x2 ha, hb, la, lb;
;             ha.x = cvt_pk_bf16(oa[0], oa[1]); ha.y = cvt_pk_bf16(oa[2], oa[3]); hb.x = cvt_pk_bf16(ob[0], ob[1]); hb.y = cvt_pk_bf16(ob[2], ob[3]);
;             la.x = cvt_pk_bf16(oa[0] - bf_lo(ha.x), oa[1] - bf_hi(ha.x)); la.y = cvt_pk_bf16(oa[2] - bf_lo(ha.y), oa[3] - bf_hi(ha.y));
;             lb.x = cvt_pk_bf16(ob[0] - bf_lo(hb.x), ob[1] - bf_hi(hb.x)); lb.y = cvt_pk_bf16(ob[2] - bf_lo(hb.y), ob[3] - bf_hi(hb.y));
;             *(u32x2*)(F.H() + (size_t)rowA * DM + col) = ha; *(u32x2*)(LO + (size_t)rowA * DM + col) = la;
;             if (hasB) { *(u32x2*)(F.H() + (size_t)rowB * DM + col) = hb; *(u32x2*)(LO + (size_t)rowB * DM + col) = lb; }
;         }
	v_mul_f32_e32 v36, v27, v27
	v_mul_f32_e32 v37, v23, v23
	v_mul_f32_e32 v41, v15, v15
	v_fmac_f32_e32 v36, v26, v26
	v_fmac_f32_e32 v37, v22, v22
	v_mul_f32_e32 v42, v3, v3
	v_fmac_f32_e32 v41, v14, v14
	v_fmac_f32_e32 v36, v28, v28
	v_fmac_f32_e32 v37, v24, v24
	v_fmac_f32_e32 v42, v2, v2
	v_fmac_f32_e32 v41, v16, v16
	v_fmac_f32_e32 v36, v29, v29
	v_fmac_f32_e32 v37, v25, v25
	v_fmac_f32_e32 v42, v4, v4
	v_fmac_f32_e32 v41, v17, v17
	v_add_f32_e32 v36, v36, v37
	v_fmac_f32_e32 v42, v5, v5
	v_add_f32_e32 v36, v36, v41
	v_add_f32_e32 v36, v36, v42
	v_mul_f32_e32 v37, v45, v45
	v_mul_f32_e32 v41, v19, v19
	v_mul_f32_e32 v42, v11, v11
	v_add_f32_dpp v36, v36, v36 quad_perm:[1,0,3,2] row_mask:0xf bank_mask:0xf bound_ctrl:1
	v_fmac_f32_e32 v37, v44, v44
	v_fmac_f32_e32 v41, v18, v18
	v_mul_f32_e32 v43, v7, v7
	v_fmac_f32_e32 v42, v10, v10
	v_add_f32_dpp v36, v36, v36 quad_perm:[2,3,0,1] row_mask:0xf bank_mask:0xf bound_ctrl:1
	v_fmac_f32_e32 v37, v46, v46
	v_fmac_f32_e32 v41, v20, v20
	v_fmac_f32_e32 v43, v6, v6
	v_fmac_f32_e32 v42, v12, v12
	v_add_f32_dpp v36, v36, v36 row_half_mirror row_mask:0xf bank_mask:0xf bound_ctrl:1
	v_fmac_f32_e32 v37, v47, v47
	v_fmac_f32_e32 v41, v21, v21
	v_fmac_f32_e32 v43, v8, v8
	v_fmac_f32_e32 v42, v13, v13
	v_add_f32_dpp v36, v36, v36 row_mirror row_mask:0xf bank_mask:0xf bound_ctrl:1
	v_add_f32_e32 v37, v37, v41
	v_fmac_f32_e32 v43, v9, v9
	v_mov_b32_e32 v41, v36
	v_add_f32_e32 v37, v37, v42
	s_nop 0
	v_permlane16_swap_b32_e32 v36, v41
	v_add_f32_e32 v42, v37, v43
	v_add_f32_e32 v37, v36, v41
	v_mov_b32_e32 v43, v37
	v_add_f32_dpp v36, v42, v42 quad_perm:[1,0,3,2] row_mask:0xf bank_mask:0xf bound_ctrl:1
	s_nop 0
	v_permlane32_swap_b32_e32 v37, v43
	v_add_f32_dpp v36, v36, v36 quad_perm:[2,3,0,1] row_mask:0xf bank_mask:0xf bound_ctrl:1
	s_nop 1
	v_add_f32_dpp v36, v36, v36 row_half_mirror row_mask:0xf bank_mask:0xf bound_ctrl:1
	s_nop 1
	v_add_f32_dpp v36, v36, v36 row_mirror row_mask:0xf bank_mask:0xf bound_ctrl:1
	v_mov_b32_e32 v41, v36
	s_nop 1
	v_permlane16_swap_b32_e32 v36, v41
	v_add_f32_e32 v36, v36, v41
	v_mov_b32_e32 v42, v36
	s_nop 1
	v_permlane32_swap_b32_e32 v36, v42
	v_pk_add_f32 v[36:37], v[36:37], v[42:43]
	v_add_f32_e32 v43, 1.0, v65
	v_pk_fma_f32 v[36:37], v[36:37], s[8:9], v[196:197] op_sel_hi:[1,0,0]
	s_nop 0
	v_mul_f32_e32 v41, 0x4b800000, v37
	v_cmp_gt_f32_e32 vcc, s3, v37
	v_cmp_gt_f32_e64 s[42:43], s3, v36
	s_nop 0
	v_cndmask_b32_e32 v37, v37, v41, vcc
	v_rsq_f32_e32 v37, v37
	v_mul_f32_e32 v41, 0x4b800000, v36
	v_cndmask_b32_e64 v36, v36, v41, s[42:43]
	v_rsq_f32_e32 v36, v36
	v_mul_f32_e32 v41, 0x45800000, v37
	v_cndmask_b32_e32 v42, v37, v41, vcc
	v_mul_f32_e32 v26, v26, v42
	v_mul_f32_e32 v37, 0x45800000, v36
	v_cndmask_b32_e64 v41, v36, v37, s[42:43]
	v_mul_f32_e32 v26, v48, v26
	v_add_f32_e32 v36, 1.0, v56
	v_fma_f32 v26, v36, v26, v52
	v_mul_f32_e32 v36, v44, v41
	v_mul_f32_e32 v36, v48, v36
	v_add_f32_e32 v37, 1.0, v64
	v_mul_f32_e32 v27, v27, v42
	v_fma_f32 v36, v37, v36, v60
	v_mul_f32_e32 v27, v49, v27
	v_add_f32_e32 v37, 1.0, v57
	v_fma_f32 v27, v37, v27, v53
	v_mul_f32_e32 v37, v45, v41
	v_mul_f32_e32 v37, v49, v37
	v_mul_f32_e32 v28, v28, v42
	v_fma_f32 v37, v43, v37, v61
	v_mul_f32_e32 v28, v50, v28
	v_add_f32_e32 v43, 1.0, v58
	v_fma_f32 v43, v43, v28, v54
	v_mul_f32_e32 v28, v46, v41
	v_mul_f32_e32 v28, v50, v28
	v_add_f32_e32 v44, 1.0, v66
	v_fma_f32 v48, v44, v28, v62
	v_mul_f32_e32 v28, v29, v42
	v_mul_f32_e32 v28, v51, v28
	v_add_f32_e32 v29, 1.0, v59
	v_cvt_pk_bf16_f32 v44, v26, v27
	v_fmac_f32_e32 v55, v29, v28
	v_lshlrev_b32_e32 v46, 16, v44
	v_mul_f32_e32 v28, v47, v41
	v_sub_f32_e32 v26, v26, v46
	v_and_b32_e32 v46, 0xffff0000, v44
	v_mul_f32_e32 v28, v51, v28
	v_add_f32_e32 v29, 1.0, v67
	v_sub_f32_e32 v27, v27, v46
	v_fmac_f32_e32 v63, v29, v28
	v_cvt_pk_bf16_f32 v45, v43, v55
	v_cvt_pk_bf16_f32 v28, v36, v37
	v_cvt_pk_bf16_f32 v29, v48, v63
	v_cvt_pk_bf16_f32 v46, v26, v27
	s_nop 0
	v_lshlrev_b32_e32 v26, 16, v45
	v_and_b32_e32 v27, 0xffff0000, v45
	v_sub_f32_e32 v26, v43, v26
	v_sub_f32_e32 v27, v55, v27
	v_cvt_pk_bf16_f32 v47, v26, v27
	v_lshlrev_b32_e32 v26, 16, v28
	v_and_b32_e32 v27, 0xffff0000, v28
	v_sub_f32_e32 v26, v36, v26
	v_sub_f32_e32 v27, v37, v27
	v_cvt_pk_bf16_f32 v36, v26, v27
	v_lshlrev_b32_e32 v26, 16, v29
	v_and_b32_e32 v27, 0xffff0000, v29
	v_sub_f32_e32 v26, v48, v26
	v_sub_f32_e32 v27, v63, v27
	v_cvt_pk_bf16_f32 v37, v26, v27
	v_lshl_add_u64 v[26:27], s[44:45], 0, v[146:147]
	v_add_co_u32_e32 v48, vcc, 0x13f16000, v26
	s_nop 1
	v_addc_co_u32_e32 v49, vcc, 0, v27, vcc
	global_store_dwordx2 v[48:49], v[44:45], off offset:256
	v_add_co_u32_e32 v44, vcc, 0x1c316000, v26
	s_nop 1
	v_addc_co_u32_e32 v45, vcc, 0, v27, vcc
	global_store_dwordx2 v[44:45], v[46:47], off offset:256
	s_cbranch_scc1 .LBB0_927
	v_lshl_add_u64 v[44:45], s[46:47], 0, v[146:147]
	v_add_co_u32_e32 v46, vcc, 0x13f16000, v44
	s_nop 1
	v_addc_co_u32_e32 v47, vcc, 0, v45, vcc
	global_store_dwordx2 v[46:47], v[28:29], off offset:256
	v_add_co_u32_e32 v28, vcc, 0x1c316000, v44
	s_nop 1
	v_addc_co_u32_e32 v29, vcc, 0, v45, vcc
	global_store_dwordx2 v[28:29], v[36:37], off offset:256
